# MoE unit queue tickets drawn 3 units ahead into a spare VGPR: no vmcnt(0) atomic round trip at each unit top
# baseline (speedup 1.0000x reference)
;     __device__ __forceinline__ void prefetch(int i) const { if (threadIdx.x == 0) tick[(base + i) & 3] = (int)__hip_atomic_fetch_add(qctr, 1u, __ATOMIC_RELAXED, __HIP_MEMORY_SCOPE_AGENT); }
; __global__ void __launch_bounds__(NWAVES * 64, 2) fwd(Args args) {
;     ...
;         S.prefetch(0); S.prefetch(1); __syncthreads();
.LBB0_1161:
	s_or_b64 exec, exec, s[8:9]
	s_waitcnt vmcnt(0)
	v_readfirstlane_b32 s4, v2
	s_nop 1
	v_add_u32_e32 v1, s4, v1
	s_add_i32 s4, 0, 0x21c04
	v_mov_b32_e32 v2, s4
	ds_write_b32 v2, v1
	v_mov_b32_e32 v251, 0
	v_mov_b32_e32 v249, 1
	s_nop 0
	global_atomic_add v250, v251, v249, s[6:7] sc0
	s_waitcnt vmcnt(0)

;     __device__ __forceinline__ void prefetch(int i) const { if (threadIdx.x == 0) tick[(base + i) & 3] = (int)__hip_atomic_fetch_add(qctr, 1u, __ATOMIC_RELAXED, __HIP_MEMORY_SCOPE_AGENT); }
; template <class Epi, class Sched>
; __device__ __forceinline__ void gemm_phase(LAS unsigned char* lds, const Sched& S, const Epi& E) {
;     ...
;         const bool has_next = S.next(ui + 1, nxt);
;         S.prefetch(ui + 2);
.LBB0_1232:
	s_and_saveexec_b64 s[18:19], s[0:1]
	s_cbranch_execz .LBB0_1236
	s_mov_b64 s[44:45], exec
	v_mbcnt_lo_u32_b32 v2, s44, 0
	v_mbcnt_hi_u32_b32 v2, s45, v2
	v_cmp_eq_u32_e32 vcc, 0, v2
	s_and_saveexec_b64 s[42:43], vcc
	s_cbranch_execz .LBB0_1235
	s_bcnt1_i32_b64 s5, s[44:45]
	v_mov_b32_e32 v3, s5
	s_waitcnt vmcnt(25)
	v_mov_b32_e32 v251, v250
	global_atomic_add v250, v149, v3, s[6:7] sc0
.LBB0_1235:
	s_or_b64 exec, exec, s[42:43]
	s_xor_b32 s5, s39, 2
	s_add_i32 s5, s5, s24
	s_and_b32 s5, s5, 3
	s_lshl_b32 s5, s5, 2
	s_add_i32 s5, s5, 0
	s_add_i32 s5, s5, 0x21c00
	v_readfirstlane_b32 s14, v251
	v_mov_b32_e32 v3, s5
	s_nop 0
	v_add_u32_e32 v2, s14, v2
	ds_write_b32 v3, v2

;     __device__ __forceinline__ void prefetch(int i) const { if (threadIdx.x == 0) tick[(base + i) & 3] = (int)__hip_atomic_fetch_add(qctr, 1u, __ATOMIC_RELAXED, __HIP_MEMORY_SCOPE_AGENT); }
; __global__ void __launch_bounds__(NWAVES * 64, 2) fwd(Args args) {
;     ...
;         S.prefetch(0); S.prefetch(1); __syncthreads();
.LBB0_1440:
	s_or_b64 exec, exec, s[8:9]
	s_waitcnt vmcnt(0)
	v_readfirstlane_b32 s6, v2
	s_nop 1
	v_add_u32_e32 v1, s6, v1
	s_add_i32 s6, 0, 0x21c04
	v_mov_b32_e32 v2, s6
	ds_write_b32 v2, v1
	v_mov_b32_e32 v251, 0
	v_mov_b32_e32 v249, 1
	s_nop 0
	global_atomic_add v250, v251, v249, s[2:3] sc0
	s_waitcnt vmcnt(0)

;     __device__ __forceinline__ void prefetch(int i) const { if (threadIdx.x == 0) tick[(base + i) & 3] = (int)__hip_atomic_fetch_add(qctr, 1u, __ATOMIC_RELAXED, __HIP_MEMORY_SCOPE_AGENT); }
; template <class Epi, class Sched>
; __device__ __forceinline__ void gemm_phase(LAS unsigned char* lds, const Sched& S, const Epi& E) {
;     ...
;         const bool has_next = S.next(ui + 1, nxt);
;         S.prefetch(ui + 2);
.LBB0_1450:
	s_and_saveexec_b64 s[10:11], s[0:1]
	s_cbranch_execz .LBB0_1454
	s_mov_b64 s[50:51], exec
	v_mbcnt_lo_u32_b32 v2, s50, 0
	v_mbcnt_hi_u32_b32 v2, s51, v2
	v_cmp_eq_u32_e32 vcc, 0, v2
	s_and_saveexec_b64 s[48:49], vcc
	s_cbranch_execz .LBB0_1453
	s_bcnt1_i32_b64 s27, s[50:51]
	v_mov_b32_e32 v3, s27
	s_waitcnt vmcnt(25)
	v_mov_b32_e32 v251, v250
	global_atomic_add v250, v147, v3, s[2:3] sc0
.LBB0_1453:
	s_or_b64 exec, exec, s[48:49]
	s_and_b32 s27, s45, 3
	s_xor_b32 s27, s27, 2
	s_lshl_b32 s27, s27, 2
	s_add_i32 s27, s27, 0
	s_add_i32 s27, s27, 0x21c00
	v_readfirstlane_b32 s31, v251
	v_mov_b32_e32 v3, s27
	s_nop 0
	v_add_u32_e32 v2, s31, v2
	ds_write_b32 v3, v2

; __global__ void __launch_bounds__(NWAVES * 64, 2) fwd(Args args) {
	.amdhsa_kernel _Z3fwd4Args
		.amdhsa_group_segment_fixed_size 0
		.amdhsa_private_segment_fixed_size 0
		.amdhsa_kernarg_size 432
		.amdhsa_user_sgpr_count 2
		.amdhsa_user_sgpr_dispatch_ptr 0
		.amdhsa_user_sgpr_queue_ptr 0
		.amdhsa_user_sgpr_kernarg_segment_ptr 1
		.amdhsa_user_sgpr_dispatch_id 0
		.amdhsa_user_sgpr_kernarg_preload_length 0
		.amdhsa_user_sgpr_kernarg_preload_offset 0
		.amdhsa_user_sgpr_private_segment_size 0
		.amdhsa_uses_dynamic_stack 0
		.amdhsa_enable_private_segment 0
		.amdhsa_system_sgpr_workgroup_id_x 1
		.amdhsa_system_sgpr_workgroup_id_y 0
		.amdhsa_system_sgpr_workgroup_id_z 0
		.amdhsa_system_sgpr_workgroup_info 0
		.amdhsa_system_vgpr_workitem_id 0
		.amdhsa_next_free_vgpr 252
		.amdhsa_next_free_sgpr 98
		.amdhsa_accum_offset 252
		.amdhsa_reserve_vcc 1
		.amdhsa_float_round_mode_32 0
		.amdhsa_float_round_mode_16_64 0
		.amdhsa_float_denorm_mode_32 3
		.amdhsa_float_denorm_mode_16_64 3
		.amdhsa_dx10_clamp 1
		.amdhsa_ieee_mode 1
		.amdhsa_fp16_overflow 0
		.amdhsa_tg_split 0
		.amdhsa_exception_fp_ieee_invalid_op 0
		.amdhsa_exception_fp_denorm_src 0
		.amdhsa_exception_fp_ieee_div_zero 0
		.amdhsa_exception_fp_ieee_overflow 0
		.amdhsa_exception_fp_ieee_underflow 0
		.amdhsa_exception_fp_ieee_inexact 0
		.amdhsa_exception_int_div_zero 0
	.end_amdhsa_kernel

; __global__ void __launch_bounds__(NWAVES * 64, 2) fwd(Args args) {
amdhsa.kernels:
  - .agpr_count:     0
    .args:
      - .offset:         0
        .size:           176
        .value_kind:     by_value
      - .offset:         176
        .size:           4
        .value_kind:     hidden_block_count_x
      - .offset:         180
        .size:           4
        .value_kind:     hidden_block_count_y
      - .offset:         184
        .size:           4
        .value_kind:     hidden_block_count_z
      - .offset:         188
        .size:           2
        .value_kind:     hidden_group_size_x
      - .offset:         190
        .size:           2
        .value_kind:     hidden_group_size_y
      - .offset:         192
        .size:           2
        .value_kind:     hidden_group_size_z
      - .offset:         194
        .size:           2
        .value_kind:     hidden_remainder_x
      - .offset:         196
        .size:           2
        .value_kind:     hidden_remainder_y
      - .offset:         198
        .size:           2
        .value_kind:     hidden_remainder_z
      - .offset:         216
        .size:           8
        .value_kind:     hidden_global_offset_x
      - .offset:         224
        .size:           8
        .value_kind:     hidden_global_offset_y
      - .offset:         232
        .size:           8
        .value_kind:     hidden_global_offset_z
      - .offset:         240
        .size:           2
        .value_kind:     hidden_grid_dims
      - .offset:         296
        .size:           4
        .value_kind:     hidden_dynamic_lds_size
    .group_segment_fixed_size: 0
    .kernarg_segment_align: 8
    .kernarg_segment_size: 432
    .language:       OpenCL C
    .language_version:
      - 2
      - 0
    .max_flat_workgroup_size: 512
    .name:           _Z3fwd4Args
    .private_segment_fixed_size: 0
    .sgpr_count:     104
    .sgpr_spill_count: 40
    .symbol:         _Z3fwd4Args.kd
    .uniform_work_group_size: 1
    .uses_dynamic_stack: false
    .vgpr_count:     252
    .vgpr_spill_count: 0
    .wavefront_size: 64
